# nt11 + GEMM3: residual x tile prefetched under the K-loop, one 16-line touch per wave per iteration (counted waits +1)
# speedup vs baseline: 1.0047x; 1.0006x over previous
;     __host__ __device__ bool next(int i, Unit& u) const {
;         const long L = (long)i * G + c; if (L >= nwg) return false;
;         int wgid = (int)L; { const int q = nwg / NXCD, r = nwg % NXCD, xcd = wgid % NXCD, off = wgid / NXCD; wgid = (xcd < r ? xcd * (q + 1) : r * (q + 1) + (xcd - r) * q) + off; }
;         const int nig = WGM * nN, gid = wgid / nig, fm = gid * WGM, gsz = (nM - fm) < WGM ? (nM - fm) : WGM;
;         u.pm = fm + ((wgid % nig) % gsz); u.pn = (wgid % nig) / gsz; return true;
;     }
.LBB0_607:
	s_lshl_b32 s98, s29, 22
	s_lshl_b32 s99, s28, 10
	s_add_u32 s98, s98, s99
	v_readlane_b32 s99, v255, 10
	s_lshl_b32 s99, s99, 19
	s_add_u32 s98, s98, s99
	s_add_u32 s98, s8, s98
	s_addc_u32 s99, s9, 0
	v_bfe_u32 v250, v202, 3, 1
	v_and_b32_e32 v251, 7, v202
	v_lshlrev_b32_e32 v250, 14, v250
	v_lshl_or_b32 v250, v251, 7, v250
	s_add_i32 s37, s37, 1
	v_readlane_b32 s22, v255, 2
	s_mul_i32 s4, s37, s46
	s_mul_hi_u32 s5, s37, s22
	s_add_i32 s5, s5, s4
	s_mul_i32 s4, s37, s22
	s_add_u32 s22, s4, s2
	s_addc_u32 s23, s5, s47
	v_cmp_gt_i64_e32 vcc, s[22:23], v[164:165]
	v_cmp_lt_i64_e64 s[4:5], s[22:23], v[162:163]
	s_cbranch_vccnz .LBB0_613
	s_ashr_i32 s23, s22, 31
	s_lshr_b32 s23, s23, 29
	s_add_i32 s58, s22, s23
	s_and_b32 s23, s58, -8
	s_sub_i32 s59, s22, s23
	s_cmp_gt_i32 s59, -1
	s_mov_b64 s[22:23], -1
	s_cbranch_scc0 .LBB0_610
	s_lshl_b32 s60, s59, 6
	s_mov_b64 s[22:23], 0

.LBB0_614:
	ds_read_b128 v[158:161], v171
	ds_read_b128 v[154:157], v171 offset:1024
	ds_read_b128 v[150:153], v171 offset:2048
	ds_read_b128 v[146:149], v171 offset:3072
	ds_read_b128 v[142:145], v172
	ds_read_b128 v[138:141], v172 offset:1024
	ds_read_b128 v[74:77], v172 offset:2048
	ds_read_b128 v[66:69], v172 offset:3072
	s_add_i32 s22, s70, 0xfff7c080
	s_cmp_eq_u32 s72, 28
	s_cselect_b32 s75, s68, s22
	s_cselect_b32 s74, s69, s71
	s_or_b32 s73, s75, 0x80
	s_mov_b32 m0, s44
	ds_read_b128 v[178:181], v173
	ds_read_b128 v[182:185], v173 offset:1024
	ds_read_b128 v[186:189], v173 offset:2048
	ds_read_b128 v[190:193], v173 offset:3072
	ds_read_b128 v[194:197], v173 offset:4096
	ds_read_b128 v[198:201], v173 offset:5120
	ds_read_b128 v[204:207], v173 offset:6144
	ds_read_b128 v[208:211], v173 offset:7168
	buffer_load_dwordx4 v1, s[16:19], s70 offen lds
	s_mov_b32 m0, s45
	s_nop 0
	buffer_load_dwordx4 v167, s[16:19], s70 offen lds
	s_waitcnt vmcnt(8)
	s_waitcnt lgkmcnt(0)
	s_barrier
	s_setprio 1
	s_waitcnt lgkmcnt(7)
	v_mfma_i32_16x16x64_i8 v[62:65], v[158:161], v[178:181], v[62:65]
	s_waitcnt lgkmcnt(6)
	v_mfma_i32_16x16x64_i8 v[62:65], v[154:157], v[182:185], v[62:65]
	v_mfma_i32_16x16x64_i8 v[50:53], v[150:153], v[178:181], v[50:53]
	s_nop 0
	v_mfma_i32_16x16x64_i8 v[50:53], v[146:149], v[182:185], v[50:53]
	s_waitcnt lgkmcnt(5)
	v_mfma_i32_16x16x64_i8 v[126:129], v[158:161], v[186:189], v[126:129]
	s_waitcnt lgkmcnt(4)
	v_mfma_i32_16x16x64_i8 v[126:129], v[154:157], v[190:193], v[126:129]
	v_mfma_i32_16x16x64_i8 v[122:125], v[150:153], v[186:189], v[122:125]
	s_nop 0
	v_mfma_i32_16x16x64_i8 v[122:125], v[146:149], v[190:193], v[122:125]
	s_waitcnt lgkmcnt(3)
	v_mfma_i32_16x16x64_i8 v[110:113], v[158:161], v[194:197], v[110:113]
	s_waitcnt lgkmcnt(2)
	v_mfma_i32_16x16x64_i8 v[110:113], v[154:157], v[198:201], v[110:113]
	v_mfma_i32_16x16x64_i8 v[106:109], v[150:153], v[194:197], v[106:109]
	s_nop 0
	v_mfma_i32_16x16x64_i8 v[106:109], v[146:149], v[198:201], v[106:109]
	s_waitcnt lgkmcnt(1)
	v_mfma_i32_16x16x64_i8 v[94:97], v[158:161], v[204:207], v[94:97]
	s_waitcnt lgkmcnt(0)
	v_mfma_i32_16x16x64_i8 v[94:97], v[154:157], v[208:211], v[94:97]
	v_mfma_i32_16x16x64_i8 v[90:93], v[150:153], v[204:207], v[90:93]
	s_nop 0
	v_mfma_i32_16x16x64_i8 v[90:93], v[146:149], v[208:211], v[90:93]
	s_setprio 0
	s_setprio 1
	v_mfma_i32_16x16x64_i8 v[134:137], v[142:145], v[178:181], v[134:137]
	s_nop 0
	v_mfma_i32_16x16x64_i8 v[134:137], v[138:141], v[182:185], v[134:137]
	v_mfma_i32_16x16x64_i8 v[130:133], v[74:77], v[178:181], v[130:133]
	s_nop 0
	v_mfma_i32_16x16x64_i8 v[130:133], v[66:69], v[182:185], v[130:133]
	v_mfma_i32_16x16x64_i8 v[118:121], v[142:145], v[186:189], v[118:121]
	s_nop 0
	v_mfma_i32_16x16x64_i8 v[118:121], v[138:141], v[190:193], v[118:121]
	v_mfma_i32_16x16x64_i8 v[114:117], v[74:77], v[186:189], v[114:117]
	s_nop 0
	v_mfma_i32_16x16x64_i8 v[114:117], v[66:69], v[190:193], v[114:117]
	v_mfma_i32_16x16x64_i8 v[102:105], v[142:145], v[194:197], v[102:105]
	s_nop 0
	v_mfma_i32_16x16x64_i8 v[102:105], v[138:141], v[198:201], v[102:105]
	v_mfma_i32_16x16x64_i8 v[98:101], v[74:77], v[194:197], v[98:101]
	s_nop 0
	v_mfma_i32_16x16x64_i8 v[98:101], v[66:69], v[198:201], v[98:101]
	v_mfma_i32_16x16x64_i8 v[86:89], v[142:145], v[204:207], v[86:89]
	s_nop 0
	v_mfma_i32_16x16x64_i8 v[86:89], v[138:141], v[208:211], v[86:89]
	v_mfma_i32_16x16x64_i8 v[82:85], v[74:77], v[204:207], v[82:85]
	s_nop 0
	v_mfma_i32_16x16x64_i8 v[82:85], v[66:69], v[208:211], v[82:85]
	s_setprio 0
	s_barrier
	s_mov_b32 m0, s27
	s_mov_b32 s22, s18
	s_mov_b32 s23, s19
	ds_read_b128 v[178:181], v173 offset:16384
	ds_read_b128 v[182:185], v173 offset:17408
	ds_read_b128 v[186:189], v173 offset:18432
	ds_read_b128 v[190:193], v173 offset:19456
	ds_read_b128 v[194:197], v173 offset:20480
	ds_read_b128 v[198:201], v173 offset:21504
	ds_read_b128 v[204:207], v173 offset:22528
	ds_read_b128 v[208:211], v173 offset:23552
	buffer_load_dwordx4 v166, s[20:23], s74 offen lds
	s_mov_b32 m0, s30
	s_add_i32 s76, s74, 0x84000
	buffer_load_dwordx4 v168, s[20:23], s74 offen lds
	s_mov_b32 m0, s31
	s_nop 0
	buffer_load_dwordx4 v166, s[20:23], s76 offen lds
	s_mov_b32 m0, s33
	s_nop 0
	buffer_load_dwordx4 v168, s[20:23], s76 offen lds
	s_mov_b32 m0, s13
	s_nop 0
	buffer_load_dwordx4 v1, s[16:19], s75 offen lds
	s_mov_b32 m0, s34
	s_nop 0
	buffer_load_dwordx4 v167, s[16:19], s75 offen lds
	global_load_dword v251, v250, s[98:99]
	s_add_u32 s98, s98, 0x8000
	s_addc_u32 s99, s99, 0
	s_waitcnt vmcnt(9)
	s_waitcnt lgkmcnt(0)
	s_barrier
	s_setprio 1
	s_waitcnt lgkmcnt(7)
	v_mfma_i32_16x16x64_i8 v[78:81], v[158:161], v[178:181], v[78:81]
	s_waitcnt lgkmcnt(6)
	v_mfma_i32_16x16x64_i8 v[78:81], v[154:157], v[182:185], v[78:81]
	v_mfma_i32_16x16x64_i8 v[70:73], v[150:153], v[178:181], v[70:73]
	s_nop 0
	v_mfma_i32_16x16x64_i8 v[70:73], v[146:149], v[182:185], v[70:73]
	s_waitcnt lgkmcnt(5)
	v_mfma_i32_16x16x64_i8 v[46:49], v[158:161], v[186:189], v[46:49]
	s_waitcnt lgkmcnt(4)
	v_mfma_i32_16x16x64_i8 v[46:49], v[154:157], v[190:193], v[46:49]
	v_mfma_i32_16x16x64_i8 v[42:45], v[150:153], v[186:189], v[42:45]
	s_nop 0
	v_mfma_i32_16x16x64_i8 v[42:45], v[146:149], v[190:193], v[42:45]
	s_waitcnt lgkmcnt(3)
	v_mfma_i32_16x16x64_i8 v[30:33], v[158:161], v[194:197], v[30:33]
	s_waitcnt lgkmcnt(2)
	v_mfma_i32_16x16x64_i8 v[30:33], v[154:157], v[198:201], v[30:33]
	v_mfma_i32_16x16x64_i8 v[26:29], v[150:153], v[194:197], v[26:29]
	s_nop 0
	v_mfma_i32_16x16x64_i8 v[26:29], v[146:149], v[198:201], v[26:29]
	s_waitcnt lgkmcnt(1)
	v_mfma_i32_16x16x64_i8 v[14:17], v[158:161], v[204:207], v[14:17]
	s_waitcnt lgkmcnt(0)
	v_mfma_i32_16x16x64_i8 v[14:17], v[154:157], v[208:211], v[14:17]
	v_mfma_i32_16x16x64_i8 v[10:13], v[150:153], v[204:207], v[10:13]
	s_nop 0
	v_mfma_i32_16x16x64_i8 v[10:13], v[146:149], v[208:211], v[10:13]
	s_setprio 0
	s_setprio 1
	v_mfma_i32_16x16x64_i8 v[58:61], v[142:145], v[178:181], v[58:61]
	s_nop 0
	v_mfma_i32_16x16x64_i8 v[58:61], v[138:141], v[182:185], v[58:61]
	v_mfma_i32_16x16x64_i8 v[54:57], v[74:77], v[178:181], v[54:57]
	s_nop 0
	v_mfma_i32_16x16x64_i8 v[54:57], v[66:69], v[182:185], v[54:57]
	v_mfma_i32_16x16x64_i8 v[38:41], v[142:145], v[186:189], v[38:41]
	s_nop 0
	v_mfma_i32_16x16x64_i8 v[38:41], v[138:141], v[190:193], v[38:41]
	v_mfma_i32_16x16x64_i8 v[34:37], v[74:77], v[186:189], v[34:37]
	s_nop 0
	v_mfma_i32_16x16x64_i8 v[34:37], v[66:69], v[190:193], v[34:37]
	v_mfma_i32_16x16x64_i8 v[22:25], v[142:145], v[194:197], v[22:25]
	s_nop 0
	v_mfma_i32_16x16x64_i8 v[22:25], v[138:141], v[198:201], v[22:25]
	v_mfma_i32_16x16x64_i8 v[18:21], v[74:77], v[194:197], v[18:21]
	s_nop 0
	v_mfma_i32_16x16x64_i8 v[18:21], v[66:69], v[198:201], v[18:21]
	v_mfma_i32_16x16x64_i8 v[6:9], v[142:145], v[204:207], v[6:9]
	s_nop 0
	v_mfma_i32_16x16x64_i8 v[6:9], v[138:141], v[208:211], v[6:9]
	v_mfma_i32_16x16x64_i8 v[2:5], v[74:77], v[204:207], v[2:5]
	s_nop 0
	v_mfma_i32_16x16x64_i8 v[2:5], v[66:69], v[208:211], v[2:5]
	s_setprio 0
	s_barrier
	ds_read_b128 v[66:69], v174
	ds_read_b128 v[74:77], v174 offset:1024
	ds_read_b128 v[138:141], v174 offset:2048
	ds_read_b128 v[142:145], v174 offset:3072
	ds_read_b128 v[146:149], v175
	ds_read_b128 v[150:153], v175 offset:1024
	ds_read_b128 v[154:157], v175 offset:2048
	ds_read_b128 v[158:161], v175 offset:3072
	s_add_i32 s75, s75, 0x84000
	s_mov_b32 m0, s35
	ds_read_b128 v[178:181], v173 offset:32768
	ds_read_b128 v[182:185], v173 offset:33792
	ds_read_b128 v[186:189], v173 offset:34816
	ds_read_b128 v[190:193], v173 offset:35840
	ds_read_b128 v[194:197], v173 offset:36864
	ds_read_b128 v[198:201], v173 offset:37888
	ds_read_b128 v[204:207], v173 offset:38912
	ds_read_b128 v[208:211], v173 offset:39936
	buffer_load_dwordx4 v1, s[16:19], s75 offen lds
	s_mov_b32 m0, s36
	s_nop 0
	buffer_load_dwordx4 v167, s[16:19], s75 offen lds
	s_waitcnt vmcnt(9)
	s_waitcnt lgkmcnt(0)
	s_barrier
	s_setprio 1
	s_waitcnt lgkmcnt(7)
	v_mfma_i32_16x16x64_i8 v[62:65], v[66:69], v[178:181], v[62:65]
	s_waitcnt lgkmcnt(6)
	v_mfma_i32_16x16x64_i8 v[62:65], v[74:77], v[182:185], v[62:65]
	v_mfma_i32_16x16x64_i8 v[50:53], v[138:141], v[178:181], v[50:53]
	s_nop 0
	v_mfma_i32_16x16x64_i8 v[50:53], v[142:145], v[182:185], v[50:53]
	s_waitcnt lgkmcnt(5)
	v_mfma_i32_16x16x64_i8 v[126:129], v[66:69], v[186:189], v[126:129]
	s_waitcnt lgkmcnt(4)
	v_mfma_i32_16x16x64_i8 v[126:129], v[74:77], v[190:193], v[126:129]
	v_mfma_i32_16x16x64_i8 v[122:125], v[138:141], v[186:189], v[122:125]
	s_nop 0
	v_mfma_i32_16x16x64_i8 v[122:125], v[142:145], v[190:193], v[122:125]
	s_waitcnt lgkmcnt(3)
	v_mfma_i32_16x16x64_i8 v[110:113], v[66:69], v[194:197], v[110:113]
	s_waitcnt lgkmcnt(2)
	v_mfma_i32_16x16x64_i8 v[110:113], v[74:77], v[198:201], v[110:113]
	v_mfma_i32_16x16x64_i8 v[106:109], v[138:141], v[194:197], v[106:109]
	s_nop 0
	v_mfma_i32_16x16x64_i8 v[106:109], v[142:145], v[198:201], v[106:109]
	s_waitcnt lgkmcnt(1)
	v_mfma_i32_16x16x64_i8 v[94:97], v[66:69], v[204:207], v[94:97]
	s_waitcnt lgkmcnt(0)
	v_mfma_i32_16x16x64_i8 v[94:97], v[74:77], v[208:211], v[94:97]
	v_mfma_i32_16x16x64_i8 v[90:93], v[138:141], v[204:207], v[90:93]
	s_nop 0
	v_mfma_i32_16x16x64_i8 v[90:93], v[142:145], v[208:211], v[90:93]
	s_setprio 0
	s_setprio 1
	v_mfma_i32_16x16x64_i8 v[134:137], v[146:149], v[178:181], v[134:137]
	s_nop 0
	v_mfma_i32_16x16x64_i8 v[134:137], v[150:153], v[182:185], v[134:137]
	v_mfma_i32_16x16x64_i8 v[130:133], v[154:157], v[178:181], v[130:133]
	s_nop 0
	v_mfma_i32_16x16x64_i8 v[130:133], v[158:161], v[182:185], v[130:133]
	v_mfma_i32_16x16x64_i8 v[118:121], v[146:149], v[186:189], v[118:121]
	s_nop 0
	v_mfma_i32_16x16x64_i8 v[118:121], v[150:153], v[190:193], v[118:121]
	v_mfma_i32_16x16x64_i8 v[114:117], v[154:157], v[186:189], v[114:117]
	s_nop 0
	v_mfma_i32_16x16x64_i8 v[114:117], v[158:161], v[190:193], v[114:117]
	v_mfma_i32_16x16x64_i8 v[102:105], v[146:149], v[194:197], v[102:105]
	s_nop 0
	v_mfma_i32_16x16x64_i8 v[102:105], v[150:153], v[198:201], v[102:105]
	v_mfma_i32_16x16x64_i8 v[98:101], v[154:157], v[194:197], v[98:101]
	s_nop 0
	v_mfma_i32_16x16x64_i8 v[98:101], v[158:161], v[198:201], v[98:101]
	v_mfma_i32_16x16x64_i8 v[86:89], v[146:149], v[204:207], v[86:89]
	s_nop 0
	v_mfma_i32_16x16x64_i8 v[86:89], v[150:153], v[208:211], v[86:89]
	v_mfma_i32_16x16x64_i8 v[82:85], v[154:157], v[204:207], v[82:85]
	s_nop 0
	v_mfma_i32_16x16x64_i8 v[82:85], v[158:161], v[208:211], v[82:85]
	s_setprio 0
	s_barrier
	s_mov_b32 m0, s38
	s_or_b32 s75, s74, 0x80
	ds_read_b128 v[178:181], v173 offset:49152
	ds_read_b128 v[182:185], v173 offset:50176
	ds_read_b128 v[186:189], v173 offset:51200
	ds_read_b128 v[190:193], v173 offset:52224
	ds_read_b128 v[194:197], v173 offset:53248
	ds_read_b128 v[198:201], v173 offset:54272
	ds_read_b128 v[204:207], v173 offset:55296
	ds_read_b128 v[208:211], v173 offset:56320
	buffer_load_dwordx4 v166, s[20:23], s75 offen lds
	s_mov_b32 m0, s39
	s_add_i32 s74, s74, 0x84080
	buffer_load_dwordx4 v168, s[20:23], s75 offen lds
	s_mov_b32 m0, s42
	s_nop 0
	buffer_load_dwordx4 v166, s[20:23], s74 offen lds
	s_mov_b32 m0, s43
	s_nop 0
	buffer_load_dwordx4 v168, s[20:23], s74 offen lds
	s_mov_b32 m0, s40
	s_nop 0
	buffer_load_dwordx4 v1, s[16:19], s73 offen lds
	s_mov_b32 m0, s41
	s_nop 0
	buffer_load_dwordx4 v167, s[16:19], s73 offen lds
	s_waitcnt vmcnt(9)
	s_waitcnt lgkmcnt(0)
	s_barrier
	s_setprio 1
	s_waitcnt lgkmcnt(7)
	v_mfma_i32_16x16x64_i8 v[78:81], v[66:69], v[178:181], v[78:81]
	s_waitcnt lgkmcnt(6)
	v_mfma_i32_16x16x64_i8 v[78:81], v[74:77], v[182:185], v[78:81]
	v_mfma_i32_16x16x64_i8 v[70:73], v[138:141], v[178:181], v[70:73]
	s_nop 0
	v_mfma_i32_16x16x64_i8 v[70:73], v[142:145], v[182:185], v[70:73]
	s_waitcnt lgkmcnt(5)
	v_mfma_i32_16x16x64_i8 v[46:49], v[66:69], v[186:189], v[46:49]
	s_waitcnt lgkmcnt(4)
	v_mfma_i32_16x16x64_i8 v[46:49], v[74:77], v[190:193], v[46:49]
	v_mfma_i32_16x16x64_i8 v[42:45], v[138:141], v[186:189], v[42:45]
	s_nop 0
	v_mfma_i32_16x16x64_i8 v[42:45], v[142:145], v[190:193], v[42:45]
	s_waitcnt lgkmcnt(3)
	v_mfma_i32_16x16x64_i8 v[30:33], v[66:69], v[194:197], v[30:33]
	s_waitcnt lgkmcnt(2)
	v_mfma_i32_16x16x64_i8 v[30:33], v[74:77], v[198:201], v[30:33]
	v_mfma_i32_16x16x64_i8 v[26:29], v[138:141], v[194:197], v[26:29]
	s_nop 0
	v_mfma_i32_16x16x64_i8 v[26:29], v[142:145], v[198:201], v[26:29]
	s_waitcnt lgkmcnt(1)
	v_mfma_i32_16x16x64_i8 v[14:17], v[66:69], v[204:207], v[14:17]
	s_waitcnt lgkmcnt(0)
	v_mfma_i32_16x16x64_i8 v[14:17], v[74:77], v[208:211], v[14:17]
	v_mfma_i32_16x16x64_i8 v[10:13], v[138:141], v[204:207], v[10:13]
	s_nop 0
	v_mfma_i32_16x16x64_i8 v[10:13], v[142:145], v[208:211], v[10:13]
	s_setprio 0
	s_setprio 1
	v_mfma_i32_16x16x64_i8 v[58:61], v[146:149], v[178:181], v[58:61]
	s_nop 0
	v_mfma_i32_16x16x64_i8 v[58:61], v[150:153], v[182:185], v[58:61]
	v_mfma_i32_16x16x64_i8 v[54:57], v[154:157], v[178:181], v[54:57]
	s_nop 0
	v_mfma_i32_16x16x64_i8 v[54:57], v[158:161], v[182:185], v[54:57]
	v_mfma_i32_16x16x64_i8 v[38:41], v[146:149], v[186:189], v[38:41]
	s_nop 0
	v_mfma_i32_16x16x64_i8 v[38:41], v[150:153], v[190:193], v[38:41]
	v_mfma_i32_16x16x64_i8 v[34:37], v[154:157], v[186:189], v[34:37]
	s_nop 0
	v_mfma_i32_16x16x64_i8 v[34:37], v[158:161], v[190:193], v[34:37]
	v_mfma_i32_16x16x64_i8 v[22:25], v[146:149], v[194:197], v[22:25]
	s_nop 0
	v_mfma_i32_16x16x64_i8 v[22:25], v[150:153], v[198:201], v[22:25]
	v_mfma_i32_16x16x64_i8 v[18:21], v[154:157], v[194:197], v[18:21]
	s_nop 0
	v_mfma_i32_16x16x64_i8 v[18:21], v[158:161], v[198:201], v[18:21]
	v_mfma_i32_16x16x64_i8 v[6:9], v[146:149], v[204:207], v[6:9]
	s_nop 0
	v_mfma_i32_16x16x64_i8 v[6:9], v[150:153], v[208:211], v[6:9]
	v_mfma_i32_16x16x64_i8 v[2:5], v[154:157], v[204:207], v[2:5]
	s_nop 0
	v_mfma_i32_16x16x64_i8 v[2:5], v[158:161], v[208:211], v[2:5]
	s_setprio 0
	s_barrier
	s_add_i32 s72, s72, 2
	s_addk_i32 s70, 0x100
	s_addk_i32 s71, 0x100
	s_cmp_gt_u32 s72, 29
	s_cbranch_scc0 .LBB0_614
	s_nop 7
	s_nop 7
	s_nop 7
	s_and_b64 vcc, exec, s[24:25]
	s_cbranch_vccz .LBB0_617
	s_barrier
